# GDN section c specialised per (role, row tile): tiles outside the causal mask are skipped, only the diagonal tile evaluates the mask; counted lgkmcnt per variant
# speedup vs baseline: 1.0409x; 1.0031x over previous
.Lgpf_done_next:
	v_and_b32_e32 v0, 15, v215
	v_lshrrev_b32_e32 v1, 4, v215
	v_readlane_b32 s0, v253, 51
	v_readlane_b32 s1, v253, 52
	v_add_u32_e32 v2, s9, v0
	v_mul_u32_u24_e32 v3, 0x110, v2
	v_lshl_add_u32 v3, v1, 4, v3
	v_mul_u32_u24_e32 v4, 0x110, v0
	v_lshl_add_u32 v4, v1, 4, v4
	v_add_u32_e32 v3, s0, v3
	v_add_u32_e32 v4, s1, v4
	s_lshl_b32 s20, s9, 2
	s_add_i32 s20, s20, 0x1c400
	v_lshl_add_u32 v5, v1, 4, s20
	v_lshlrev_b32_e32 v6, 2, v0
	v_add_u32_e32 v6, 0x1c400, v6
	ds_read_b128 v[40:43], v3
	ds_read_b128 v[44:47], v3 offset:64
	ds_read_b128 v[48:51], v3 offset:128
	ds_read_b128 v[52:55], v3 offset:192
	s_and_b32 s34, s56, 0x80000000
	s_xor_b32 s34, s34, 0x3fb8aa3b
	s_cmp_lg_u32 s56, 0
	s_cbranch_scc1 .Lgc_s1
	s_cmp_eq_u32 s9, 16
	s_cbranch_scc1 .Lgc_v0_1
	s_cmp_eq_u32 s9, 32
	s_cbranch_scc1 .Lgc_v0_2
	s_cmp_eq_u32 s9, 48
	s_cbranch_scc1 .Lgc_v0_3
	s_branch .Lgc_v0_0
.Lgc_s1:
	s_cmp_eq_u32 s9, 16
	s_cbranch_scc1 .Lgc_v1_1
	s_cmp_eq_u32 s9, 32
	s_cbranch_scc1 .Lgc_v1_2
	s_cmp_eq_u32 s9, 48
	s_cbranch_scc1 .Lgc_v1_3
	s_branch .Lgc_v1_0
.Lgc_v0_0:
	ds_read_b128 v[56:59], v4
	ds_read_b128 v[60:63], v4 offset:64
	ds_read_b128 v[64:67], v4 offset:128
	ds_read_b128 v[68:71], v4 offset:192
	ds_read_b128 v[144:147], v5
	ds_read_b32 v136, v6
	v_lshl_add_u32 v12, v1, 2, s9
	v_add_u32_e32 v13, 1, v12
	v_add_u32_e32 v14, 2, v12
	v_add_u32_e32 v15, 3, v12
	v_mov_b32_e32 v152, 0
	v_mov_b32_e32 v153, 0
	v_mov_b32_e32 v154, 0
	v_mov_b32_e32 v155, 0
	v_mov_b32_e32 v156, 0
	v_mov_b32_e32 v157, 0
	v_mov_b32_e32 v158, 0
	v_mov_b32_e32 v159, 0
	v_mov_b32_e32 v160, 0
	v_mov_b32_e32 v161, 0
	v_mov_b32_e32 v162, 0
	v_mov_b32_e32 v163, 0
	s_waitcnt lgkmcnt(0)
	v_mfma_f32_16x16x32_bf16 v[120:123], v[40:43], v[56:59], 0
	v_mfma_f32_16x16x32_bf16 v[120:123], v[44:47], v[60:63], v[120:123]
	v_mfma_f32_16x16x32_bf16 v[120:123], v[48:51], v[64:67], v[120:123]
	v_mfma_f32_16x16x32_bf16 v[120:123], v[52:55], v[68:71], v[120:123]
	v_sub_f32_e32 v148, v144, v136
	v_sub_f32_e32 v149, v145, v136
	v_sub_f32_e32 v150, v146, v136
	v_sub_f32_e32 v151, v147, v136
	v_mul_f32_e32 v148, s34, v148
	v_mul_f32_e32 v149, s34, v149
	v_mul_f32_e32 v150, s34, v150
	v_mul_f32_e32 v151, s34, v151
	v_exp_f32_e32 v148, v148
	v_exp_f32_e32 v149, v149
	v_exp_f32_e32 v150, v150
	v_exp_f32_e32 v151, v151
	v_mul_f32_e32 v148, v120, v148
	v_mul_f32_e32 v149, v121, v149
	v_mul_f32_e32 v150, v122, v150
	v_mul_f32_e32 v151, v123, v151
	v_cmp_lt_i32_e32 vcc, v0, v12
	v_cmp_lt_i32_e64 s[0:1], v0, v13
	v_cmp_lt_i32_e64 s[20:21], v0, v14
	v_cndmask_b32_e32 v148, 0, v148, vcc
	v_cmp_lt_i32_e32 vcc, v0, v15
	v_cndmask_b32_e64 v149, 0, v149, s[0:1]
	v_cndmask_b32_e64 v150, 0, v150, s[20:21]
	s_nop 0
	v_cndmask_b32_e32 v151, 0, v151, vcc
	s_branch .Lgc_st0
.Lgc_v0_1:
	ds_read_b128 v[56:59], v4
	ds_read_b128 v[60:63], v4 offset:64
	ds_read_b128 v[64:67], v4 offset:128
	ds_read_b128 v[68:71], v4 offset:192
	ds_read_b128 v[144:147], v5
	ds_read_b32 v136, v6
	ds_read_b32 v137, v6 offset:64
	ds_read_b128 v[72:75], v4 offset:4352
	ds_read_b128 v[76:79], v4 offset:4416
	ds_read_b128 v[80:83], v4 offset:4480
	ds_read_b128 v[84:87], v4 offset:4544
	v_add_u32_e32 v9, 16, v0
	v_lshl_add_u32 v12, v1, 2, s9
	v_add_u32_e32 v13, 1, v12
	v_add_u32_e32 v14, 2, v12
	v_add_u32_e32 v15, 3, v12
	v_mov_b32_e32 v156, 0
	v_mov_b32_e32 v157, 0
	v_mov_b32_e32 v158, 0
	v_mov_b32_e32 v159, 0
	v_mov_b32_e32 v160, 0
	v_mov_b32_e32 v161, 0
	v_mov_b32_e32 v162, 0
	v_mov_b32_e32 v163, 0
	s_waitcnt lgkmcnt(5)
	v_mfma_f32_16x16x32_bf16 v[120:123], v[40:43], v[56:59], 0
	v_mfma_f32_16x16x32_bf16 v[120:123], v[44:47], v[60:63], v[120:123]
	v_mfma_f32_16x16x32_bf16 v[120:123], v[48:51], v[64:67], v[120:123]
	v_mfma_f32_16x16x32_bf16 v[120:123], v[52:55], v[68:71], v[120:123]
	v_sub_f32_e32 v148, v144, v136
	v_sub_f32_e32 v149, v145, v136
	v_sub_f32_e32 v150, v146, v136
	v_sub_f32_e32 v151, v147, v136
	v_mul_f32_e32 v148, s34, v148
	v_mul_f32_e32 v149, s34, v149
	v_mul_f32_e32 v150, s34, v150
	v_mul_f32_e32 v151, s34, v151
	v_exp_f32_e32 v148, v148
	v_exp_f32_e32 v149, v149
	v_exp_f32_e32 v150, v150
	v_exp_f32_e32 v151, v151
	s_waitcnt lgkmcnt(0)
	v_mfma_f32_16x16x32_bf16 v[124:127], v[40:43], v[72:75], 0
	v_mfma_f32_16x16x32_bf16 v[124:127], v[44:47], v[76:79], v[124:127]
	v_mfma_f32_16x16x32_bf16 v[124:127], v[48:51], v[80:83], v[124:127]
	v_mfma_f32_16x16x32_bf16 v[124:127], v[52:55], v[84:87], v[124:127]
	v_mul_f32_e32 v148, v120, v148
	v_mul_f32_e32 v149, v121, v149
	v_mul_f32_e32 v150, v122, v150
	v_mul_f32_e32 v151, v123, v151
	v_sub_f32_e32 v152, v144, v137
	v_sub_f32_e32 v153, v145, v137
	v_sub_f32_e32 v154, v146, v137
	v_sub_f32_e32 v155, v147, v137
	v_mul_f32_e32 v152, s34, v152
	v_mul_f32_e32 v153, s34, v153
	v_mul_f32_e32 v154, s34, v154
	v_mul_f32_e32 v155, s34, v155
	v_exp_f32_e32 v152, v152
	v_exp_f32_e32 v153, v153
	v_exp_f32_e32 v154, v154
	v_exp_f32_e32 v155, v155
	v_mul_f32_e32 v152, v124, v152
	v_mul_f32_e32 v153, v125, v153
	v_mul_f32_e32 v154, v126, v154
	v_mul_f32_e32 v155, v127, v155
	v_cmp_lt_i32_e32 vcc, v9, v12
	v_cmp_lt_i32_e64 s[0:1], v9, v13
	v_cmp_lt_i32_e64 s[20:21], v9, v14
	v_cndmask_b32_e32 v152, 0, v152, vcc
	v_cmp_lt_i32_e32 vcc, v9, v15
	v_cndmask_b32_e64 v153, 0, v153, s[0:1]
	v_cndmask_b32_e64 v154, 0, v154, s[20:21]
	s_nop 0
	v_cndmask_b32_e32 v155, 0, v155, vcc
	s_branch .Lgc_st0
.Lgc_v0_2:
	ds_read_b128 v[56:59], v4
	ds_read_b128 v[60:63], v4 offset:64
	ds_read_b128 v[64:67], v4 offset:128
	ds_read_b128 v[68:71], v4 offset:192
	ds_read_b128 v[144:147], v5
	ds_read_b32 v136, v6
	ds_read_b32 v137, v6 offset:64
	ds_read_b32 v138, v6 offset:128
	ds_read_b128 v[72:75], v4 offset:4352
	ds_read_b128 v[76:79], v4 offset:4416
	ds_read_b128 v[80:83], v4 offset:4480
	ds_read_b128 v[84:87], v4 offset:4544
	ds_read_b128 v[88:91], v4 offset:8704
	ds_read_b128 v[92:95], v4 offset:8768
	ds_read_b128 v[96:99], v4 offset:8832
	ds_read_b128 v[100:103], v4 offset:8896
	v_add_u32_e32 v10, 32, v0
	v_lshl_add_u32 v12, v1, 2, s9
	v_add_u32_e32 v13, 1, v12
	v_add_u32_e32 v14, 2, v12
	v_add_u32_e32 v15, 3, v12
	v_mov_b32_e32 v160, 0
	v_mov_b32_e32 v161, 0
	v_mov_b32_e32 v162, 0
	v_mov_b32_e32 v163, 0
	s_waitcnt lgkmcnt(10)
	v_mfma_f32_16x16x32_bf16 v[120:123], v[40:43], v[56:59], 0
	v_mfma_f32_16x16x32_bf16 v[120:123], v[44:47], v[60:63], v[120:123]
	v_mfma_f32_16x16x32_bf16 v[120:123], v[48:51], v[64:67], v[120:123]
	v_mfma_f32_16x16x32_bf16 v[120:123], v[52:55], v[68:71], v[120:123]
	v_sub_f32_e32 v148, v144, v136
	v_sub_f32_e32 v149, v145, v136
	v_sub_f32_e32 v150, v146, v136
	v_sub_f32_e32 v151, v147, v136
	v_mul_f32_e32 v148, s34, v148
	v_mul_f32_e32 v149, s34, v149
	v_mul_f32_e32 v150, s34, v150
	v_mul_f32_e32 v151, s34, v151
	v_exp_f32_e32 v148, v148
	v_exp_f32_e32 v149, v149
	v_exp_f32_e32 v150, v150
	v_exp_f32_e32 v151, v151
	s_waitcnt lgkmcnt(4)
	v_mfma_f32_16x16x32_bf16 v[124:127], v[40:43], v[72:75], 0
	v_mfma_f32_16x16x32_bf16 v[124:127], v[44:47], v[76:79], v[124:127]
	v_mfma_f32_16x16x32_bf16 v[124:127], v[48:51], v[80:83], v[124:127]
	v_mfma_f32_16x16x32_bf16 v[124:127], v[52:55], v[84:87], v[124:127]
	v_mul_f32_e32 v148, v120, v148
	v_mul_f32_e32 v149, v121, v149
	v_mul_f32_e32 v150, v122, v150
	v_mul_f32_e32 v151, v123, v151
	v_sub_f32_e32 v152, v144, v137
	v_sub_f32_e32 v153, v145, v137
	v_sub_f32_e32 v154, v146, v137
	v_sub_f32_e32 v155, v147, v137
	v_mul_f32_e32 v152, s34, v152
	v_mul_f32_e32 v153, s34, v153
	v_mul_f32_e32 v154, s34, v154
	v_mul_f32_e32 v155, s34, v155
	v_exp_f32_e32 v152, v152
	v_exp_f32_e32 v153, v153
	v_exp_f32_e32 v154, v154
	v_exp_f32_e32 v155, v155
	s_waitcnt lgkmcnt(0)
	v_mfma_f32_16x16x32_bf16 v[128:131], v[40:43], v[88:91], 0
	v_mfma_f32_16x16x32_bf16 v[128:131], v[44:47], v[92:95], v[128:131]
	v_mfma_f32_16x16x32_bf16 v[128:131], v[48:51], v[96:99], v[128:131]
	v_mfma_f32_16x16x32_bf16 v[128:131], v[52:55], v[100:103], v[128:131]
	v_mul_f32_e32 v152, v124, v152
	v_mul_f32_e32 v153, v125, v153
	v_mul_f32_e32 v154, v126, v154
	v_mul_f32_e32 v155, v127, v155
	v_sub_f32_e32 v156, v144, v138
	v_sub_f32_e32 v157, v145, v138
	v_sub_f32_e32 v158, v146, v138
	v_sub_f32_e32 v159, v147, v138
	v_mul_f32_e32 v156, s34, v156
	v_mul_f32_e32 v157, s34, v157
	v_mul_f32_e32 v158, s34, v158
	v_mul_f32_e32 v159, s34, v159
	v_exp_f32_e32 v156, v156
	v_exp_f32_e32 v157, v157
	v_exp_f32_e32 v158, v158
	v_exp_f32_e32 v159, v159
	v_mul_f32_e32 v156, v128, v156
	v_mul_f32_e32 v157, v129, v157
	v_mul_f32_e32 v158, v130, v158
	v_mul_f32_e32 v159, v131, v159
	v_cmp_lt_i32_e32 vcc, v10, v12
	v_cmp_lt_i32_e64 s[0:1], v10, v13
	v_cmp_lt_i32_e64 s[20:21], v10, v14
	v_cndmask_b32_e32 v156, 0, v156, vcc
	v_cmp_lt_i32_e32 vcc, v10, v15
	v_cndmask_b32_e64 v157, 0, v157, s[0:1]
	v_cndmask_b32_e64 v158, 0, v158, s[20:21]
	s_nop 0
	v_cndmask_b32_e32 v159, 0, v159, vcc
	s_branch .Lgc_st0
.Lgc_v0_3:
	ds_read_b128 v[56:59], v4
	ds_read_b128 v[60:63], v4 offset:64
	ds_read_b128 v[64:67], v4 offset:128
	ds_read_b128 v[68:71], v4 offset:192
	ds_read_b128 v[144:147], v5
	ds_read_b32 v136, v6
	ds_read_b32 v137, v6 offset:64
	ds_read_b32 v138, v6 offset:128
	ds_read_b32 v139, v6 offset:192
	ds_read_b128 v[72:75], v4 offset:4352
	ds_read_b128 v[76:79], v4 offset:4416
	ds_read_b128 v[80:83], v4 offset:4480
	ds_read_b128 v[84:87], v4 offset:4544
	ds_read_b128 v[88:91], v4 offset:8704
	ds_read_b128 v[92:95], v4 offset:8768
	ds_read_b128 v[96:99], v4 offset:8832
	ds_read_b128 v[100:103], v4 offset:8896
	ds_read_b128 v[104:107], v4 offset:13056
	ds_read_b128 v[108:111], v4 offset:13120
	ds_read_b128 v[112:115], v4 offset:13184
	ds_read_b128 v[116:119], v4 offset:13248
	v_add_u32_e32 v11, 48, v0
	v_lshl_add_u32 v12, v1, 2, s9
	v_add_u32_e32 v13, 1, v12
	v_add_u32_e32 v14, 2, v12
	v_add_u32_e32 v15, 3, v12
	s_waitcnt lgkmcnt(15)
	v_mfma_f32_16x16x32_bf16 v[120:123], v[40:43], v[56:59], 0
	v_mfma_f32_16x16x32_bf16 v[120:123], v[44:47], v[60:63], v[120:123]
	v_mfma_f32_16x16x32_bf16 v[120:123], v[48:51], v[64:67], v[120:123]
	v_mfma_f32_16x16x32_bf16 v[120:123], v[52:55], v[68:71], v[120:123]
	v_sub_f32_e32 v148, v144, v136
	v_sub_f32_e32 v149, v145, v136
	v_sub_f32_e32 v150, v146, v136
	v_sub_f32_e32 v151, v147, v136
	v_mul_f32_e32 v148, s34, v148
	v_mul_f32_e32 v149, s34, v149
	v_mul_f32_e32 v150, s34, v150
	v_mul_f32_e32 v151, s34, v151
	v_exp_f32_e32 v148, v148
	v_exp_f32_e32 v149, v149
	v_exp_f32_e32 v150, v150
	v_exp_f32_e32 v151, v151
	s_waitcnt lgkmcnt(8)
	v_mfma_f32_16x16x32_bf16 v[124:127], v[40:43], v[72:75], 0
	v_mfma_f32_16x16x32_bf16 v[124:127], v[44:47], v[76:79], v[124:127]
	v_mfma_f32_16x16x32_bf16 v[124:127], v[48:51], v[80:83], v[124:127]
	v_mfma_f32_16x16x32_bf16 v[124:127], v[52:55], v[84:87], v[124:127]
	v_mul_f32_e32 v148, v120, v148
	v_mul_f32_e32 v149, v121, v149
	v_mul_f32_e32 v150, v122, v150
	v_mul_f32_e32 v151, v123, v151
	v_sub_f32_e32 v152, v144, v137
	v_sub_f32_e32 v153, v145, v137
	v_sub_f32_e32 v154, v146, v137
	v_sub_f32_e32 v155, v147, v137
	v_mul_f32_e32 v152, s34, v152
	v_mul_f32_e32 v153, s34, v153
	v_mul_f32_e32 v154, s34, v154
	v_mul_f32_e32 v155, s34, v155
	v_exp_f32_e32 v152, v152
	v_exp_f32_e32 v153, v153
	v_exp_f32_e32 v154, v154
	v_exp_f32_e32 v155, v155
	s_waitcnt lgkmcnt(4)
	v_mfma_f32_16x16x32_bf16 v[128:131], v[40:43], v[88:91], 0
	v_mfma_f32_16x16x32_bf16 v[128:131], v[44:47], v[92:95], v[128:131]
	v_mfma_f32_16x16x32_bf16 v[128:131], v[48:51], v[96:99], v[128:131]
	v_mfma_f32_16x16x32_bf16 v[128:131], v[52:55], v[100:103], v[128:131]
	v_mul_f32_e32 v152, v124, v152
	v_mul_f32_e32 v153, v125, v153
	v_mul_f32_e32 v154, v126, v154
	v_mul_f32_e32 v155, v127, v155
	v_sub_f32_e32 v156, v144, v138
	v_sub_f32_e32 v157, v145, v138
	v_sub_f32_e32 v158, v146, v138
	v_sub_f32_e32 v159, v147, v138
	v_mul_f32_e32 v156, s34, v156
	v_mul_f32_e32 v157, s34, v157
	v_mul_f32_e32 v158, s34, v158
	v_mul_f32_e32 v159, s34, v159
	v_exp_f32_e32 v156, v156
	v_exp_f32_e32 v157, v157
	v_exp_f32_e32 v158, v158
	v_exp_f32_e32 v159, v159
	s_waitcnt lgkmcnt(0)
	v_mfma_f32_16x16x32_bf16 v[132:135], v[40:43], v[104:107], 0
	v_mfma_f32_16x16x32_bf16 v[132:135], v[44:47], v[108:111], v[132:135]
	v_mfma_f32_16x16x32_bf16 v[132:135], v[48:51], v[112:115], v[132:135]
	v_mfma_f32_16x16x32_bf16 v[132:135], v[52:55], v[116:119], v[132:135]
	v_mul_f32_e32 v156, v128, v156
	v_mul_f32_e32 v157, v129, v157
	v_mul_f32_e32 v158, v130, v158
	v_mul_f32_e32 v159, v131, v159
	v_sub_f32_e32 v160, v144, v139
	v_sub_f32_e32 v161, v145, v139
	v_sub_f32_e32 v162, v146, v139
	v_sub_f32_e32 v163, v147, v139
	v_mul_f32_e32 v160, s34, v160
	v_mul_f32_e32 v161, s34, v161
	v_mul_f32_e32 v162, s34, v162
	v_mul_f32_e32 v163, s34, v163
	v_exp_f32_e32 v160, v160
	v_exp_f32_e32 v161, v161
	v_exp_f32_e32 v162, v162
	v_exp_f32_e32 v163, v163
	v_mul_f32_e32 v160, v132, v160
	v_mul_f32_e32 v161, v133, v161
	v_mul_f32_e32 v162, v134, v162
	v_mul_f32_e32 v163, v135, v163
	v_cmp_lt_i32_e32 vcc, v11, v12
	v_cmp_lt_i32_e64 s[0:1], v11, v13
	v_cmp_lt_i32_e64 s[20:21], v11, v14
	v_cndmask_b32_e32 v160, 0, v160, vcc
	v_cmp_lt_i32_e32 vcc, v11, v15
	v_cndmask_b32_e64 v161, 0, v161, s[0:1]
	v_cndmask_b32_e64 v162, 0, v162, s[20:21]
	s_nop 0
	v_cndmask_b32_e32 v163, 0, v163, vcc
	s_branch .Lgc_st0
.Lgc_v1_0:
	ds_read_b128 v[56:59], v4
	ds_read_b128 v[60:63], v4 offset:64
	ds_read_b128 v[64:67], v4 offset:128
	ds_read_b128 v[68:71], v4 offset:192
	ds_read_b128 v[144:147], v5
	ds_read_b32 v136, v6
	ds_read_b32 v137, v6 offset:64
	ds_read_b32 v138, v6 offset:128
	ds_read_b32 v139, v6 offset:192
	ds_read_b128 v[72:75], v4 offset:4352
	ds_read_b128 v[76:79], v4 offset:4416
	ds_read_b128 v[80:83], v4 offset:4480
	ds_read_b128 v[84:87], v4 offset:4544
	ds_read_b128 v[88:91], v4 offset:8704
	ds_read_b128 v[92:95], v4 offset:8768
	ds_read_b128 v[96:99], v4 offset:8832
	ds_read_b128 v[100:103], v4 offset:8896
	ds_read_b128 v[104:107], v4 offset:13056
	ds_read_b128 v[108:111], v4 offset:13120
	ds_read_b128 v[112:115], v4 offset:13184
	ds_read_b128 v[116:119], v4 offset:13248
	v_lshl_add_u32 v12, v1, 2, s9
	v_add_u32_e32 v13, 1, v12
	v_add_u32_e32 v14, 2, v12
	v_add_u32_e32 v15, 3, v12
	s_waitcnt lgkmcnt(15)
	v_mfma_f32_16x16x32_bf16 v[120:123], v[40:43], v[56:59], 0
	v_mfma_f32_16x16x32_bf16 v[120:123], v[44:47], v[60:63], v[120:123]
	v_mfma_f32_16x16x32_bf16 v[120:123], v[48:51], v[64:67], v[120:123]
	v_mfma_f32_16x16x32_bf16 v[120:123], v[52:55], v[68:71], v[120:123]
	v_sub_f32_e32 v148, v144, v136
	v_sub_f32_e32 v149, v145, v136
	v_sub_f32_e32 v150, v146, v136
	v_sub_f32_e32 v151, v147, v136
	v_mul_f32_e32 v148, s34, v148
	v_mul_f32_e32 v149, s34, v149
	v_mul_f32_e32 v150, s34, v150
	v_mul_f32_e32 v151, s34, v151
	v_exp_f32_e32 v148, v148
	v_exp_f32_e32 v149, v149
	v_exp_f32_e32 v150, v150
	v_exp_f32_e32 v151, v151
	s_waitcnt lgkmcnt(8)
	v_mfma_f32_16x16x32_bf16 v[124:127], v[40:43], v[72:75], 0
	v_mfma_f32_16x16x32_bf16 v[124:127], v[44:47], v[76:79], v[124:127]
	v_mfma_f32_16x16x32_bf16 v[124:127], v[48:51], v[80:83], v[124:127]
	v_mfma_f32_16x16x32_bf16 v[124:127], v[52:55], v[84:87], v[124:127]
	v_mul_f32_e32 v148, v120, v148
	v_mul_f32_e32 v149, v121, v149
	v_mul_f32_e32 v150, v122, v150
	v_mul_f32_e32 v151, v123, v151
	v_cmp_le_i32_e32 vcc, v12, v0
	v_cmp_le_i32_e64 s[0:1], v13, v0
	v_cmp_le_i32_e64 s[20:21], v14, v0
	v_cndmask_b32_e32 v148, 0, v148, vcc
	v_cmp_le_i32_e32 vcc, v15, v0
	v_cndmask_b32_e64 v149, 0, v149, s[0:1]
	v_cndmask_b32_e64 v150, 0, v150, s[20:21]
	s_nop 0
	v_cndmask_b32_e32 v151, 0, v151, vcc
	v_sub_f32_e32 v152, v144, v137
	v_sub_f32_e32 v153, v145, v137
	v_sub_f32_e32 v154, v146, v137
	v_sub_f32_e32 v155, v147, v137
	v_mul_f32_e32 v152, s34, v152
	v_mul_f32_e32 v153, s34, v153
	v_mul_f32_e32 v154, s34, v154
	v_mul_f32_e32 v155, s34, v155
	v_exp_f32_e32 v152, v152
	v_exp_f32_e32 v153, v153
	v_exp_f32_e32 v154, v154
	v_exp_f32_e32 v155, v155
	s_waitcnt lgkmcnt(4)
	v_mfma_f32_16x16x32_bf16 v[128:131], v[40:43], v[88:91], 0
	v_mfma_f32_16x16x32_bf16 v[128:131], v[44:47], v[92:95], v[128:131]
	v_mfma_f32_16x16x32_bf16 v[128:131], v[48:51], v[96:99], v[128:131]
	v_mfma_f32_16x16x32_bf16 v[128:131], v[52:55], v[100:103], v[128:131]
	v_mul_f32_e32 v152, v124, v152
	v_mul_f32_e32 v153, v125, v153
	v_mul_f32_e32 v154, v126, v154
	v_mul_f32_e32 v155, v127, v155
	v_sub_f32_e32 v156, v144, v138
	v_sub_f32_e32 v157, v145, v138
	v_sub_f32_e32 v158, v146, v138
	v_sub_f32_e32 v159, v147, v138
	v_mul_f32_e32 v156, s34, v156
	v_mul_f32_e32 v157, s34, v157
	v_mul_f32_e32 v158, s34, v158
	v_mul_f32_e32 v159, s34, v159
	v_exp_f32_e32 v156, v156
	v_exp_f32_e32 v157, v157
	v_exp_f32_e32 v158, v158
	v_exp_f32_e32 v159, v159
	s_waitcnt lgkmcnt(0)
	v_mfma_f32_16x16x32_bf16 v[132:135], v[40:43], v[104:107], 0
	v_mfma_f32_16x16x32_bf16 v[132:135], v[44:47], v[108:111], v[132:135]
	v_mfma_f32_16x16x32_bf16 v[132:135], v[48:51], v[112:115], v[132:135]
	v_mfma_f32_16x16x32_bf16 v[132:135], v[52:55], v[116:119], v[132:135]
	v_mul_f32_e32 v156, v128, v156
	v_mul_f32_e32 v157, v129, v157
	v_mul_f32_e32 v158, v130, v158
	v_mul_f32_e32 v159, v131, v159
	v_sub_f32_e32 v160, v144, v139
	v_sub_f32_e32 v161, v145, v139
	v_sub_f32_e32 v162, v146, v139
	v_sub_f32_e32 v163, v147, v139
	v_mul_f32_e32 v160, s34, v160
	v_mul_f32_e32 v161, s34, v161
	v_mul_f32_e32 v162, s34, v162
	v_mul_f32_e32 v163, s34, v163
	v_exp_f32_e32 v160, v160
	v_exp_f32_e32 v161, v161
	v_exp_f32_e32 v162, v162
	v_exp_f32_e32 v163, v163
	v_mul_f32_e32 v160, v132, v160
	v_mul_f32_e32 v161, v133, v161
	v_mul_f32_e32 v162, v134, v162
	v_mul_f32_e32 v163, v135, v163
	s_branch .Lgc_st1
.Lgc_v1_1:
	ds_read_b128 v[72:75], v4 offset:4352
	ds_read_b128 v[76:79], v4 offset:4416
	ds_read_b128 v[80:83], v4 offset:4480
	ds_read_b128 v[84:87], v4 offset:4544
	ds_read_b128 v[144:147], v5
	ds_read_b32 v137, v6 offset:64
	ds_read_b32 v138, v6 offset:128
	ds_read_b32 v139, v6 offset:192
	ds_read_b128 v[88:91], v4 offset:8704
	ds_read_b128 v[92:95], v4 offset:8768
	ds_read_b128 v[96:99], v4 offset:8832
	ds_read_b128 v[100:103], v4 offset:8896
	ds_read_b128 v[104:107], v4 offset:13056
	ds_read_b128 v[108:111], v4 offset:13120
	ds_read_b128 v[112:115], v4 offset:13184
	ds_read_b128 v[116:119], v4 offset:13248
	v_add_u32_e32 v9, 16, v0
	v_lshl_add_u32 v12, v1, 2, s9
	v_add_u32_e32 v13, 1, v12
	v_add_u32_e32 v14, 2, v12
	v_add_u32_e32 v15, 3, v12
	v_mov_b32_e32 v148, 0
	v_mov_b32_e32 v149, 0
	v_mov_b32_e32 v150, 0
	v_mov_b32_e32 v151, 0
	s_waitcnt lgkmcnt(10)
	v_mfma_f32_16x16x32_bf16 v[124:127], v[40:43], v[72:75], 0
	v_mfma_f32_16x16x32_bf16 v[124:127], v[44:47], v[76:79], v[124:127]
	v_mfma_f32_16x16x32_bf16 v[124:127], v[48:51], v[80:83], v[124:127]
	v_mfma_f32_16x16x32_bf16 v[124:127], v[52:55], v[84:87], v[124:127]
	v_sub_f32_e32 v152, v144, v137
	v_sub_f32_e32 v153, v145, v137
	v_sub_f32_e32 v154, v146, v137
	v_sub_f32_e32 v155, v147, v137
	v_mul_f32_e32 v152, s34, v152
	v_mul_f32_e32 v153, s34, v153
	v_mul_f32_e32 v154, s34, v154
	v_mul_f32_e32 v155, s34, v155
	v_exp_f32_e32 v152, v152
	v_exp_f32_e32 v153, v153
	v_exp_f32_e32 v154, v154
	v_exp_f32_e32 v155, v155
	s_waitcnt lgkmcnt(4)
	v_mfma_f32_16x16x32_bf16 v[128:131], v[40:43], v[88:91], 0
	v_mfma_f32_16x16x32_bf16 v[128:131], v[44:47], v[92:95], v[128:131]
	v_mfma_f32_16x16x32_bf16 v[128:131], v[48:51], v[96:99], v[128:131]
	v_mfma_f32_16x16x32_bf16 v[128:131], v[52:55], v[100:103], v[128:131]
	v_mul_f32_e32 v152, v124, v152
	v_mul_f32_e32 v153, v125, v153
	v_mul_f32_e32 v154, v126, v154
	v_mul_f32_e32 v155, v127, v155
	v_cmp_le_i32_e32 vcc, v12, v9
	v_cmp_le_i32_e64 s[0:1], v13, v9
	v_cmp_le_i32_e64 s[20:21], v14, v9
	v_cndmask_b32_e32 v152, 0, v152, vcc
	v_cmp_le_i32_e32 vcc, v15, v9
	v_cndmask_b32_e64 v153, 0, v153, s[0:1]
	v_cndmask_b32_e64 v154, 0, v154, s[20:21]
	s_nop 0
	v_cndmask_b32_e32 v155, 0, v155, vcc
	v_sub_f32_e32 v156, v144, v138
	v_sub_f32_e32 v157, v145, v138
	v_sub_f32_e32 v158, v146, v138
	v_sub_f32_e32 v159, v147, v138
	v_mul_f32_e32 v156, s34, v156
	v_mul_f32_e32 v157, s34, v157
	v_mul_f32_e32 v158, s34, v158
	v_mul_f32_e32 v159, s34, v159
	v_exp_f32_e32 v156, v156
	v_exp_f32_e32 v157, v157
	v_exp_f32_e32 v158, v158
	v_exp_f32_e32 v159, v159
	s_waitcnt lgkmcnt(0)
	v_mfma_f32_16x16x32_bf16 v[132:135], v[40:43], v[104:107], 0
	v_mfma_f32_16x16x32_bf16 v[132:135], v[44:47], v[108:111], v[132:135]
	v_mfma_f32_16x16x32_bf16 v[132:135], v[48:51], v[112:115], v[132:135]
	v_mfma_f32_16x16x32_bf16 v[132:135], v[52:55], v[116:119], v[132:135]
	v_mul_f32_e32 v156, v128, v156
	v_mul_f32_e32 v157, v129, v157
	v_mul_f32_e32 v158, v130, v158
	v_mul_f32_e32 v159, v131, v159
	v_sub_f32_e32 v160, v144, v139
	v_sub_f32_e32 v161, v145, v139
	v_sub_f32_e32 v162, v146, v139
	v_sub_f32_e32 v163, v147, v139
	v_mul_f32_e32 v160, s34, v160
	v_mul_f32_e32 v161, s34, v161
	v_mul_f32_e32 v162, s34, v162
	v_mul_f32_e32 v163, s34, v163
	v_exp_f32_e32 v160, v160
	v_exp_f32_e32 v161, v161
	v_exp_f32_e32 v162, v162
	v_exp_f32_e32 v163, v163
	v_mul_f32_e32 v160, v132, v160
	v_mul_f32_e32 v161, v133, v161
	v_mul_f32_e32 v162, v134, v162
	v_mul_f32_e32 v163, v135, v163
	s_branch .Lgc_st1
.Lgc_v1_2:
	ds_read_b128 v[88:91], v4 offset:8704
	ds_read_b128 v[92:95], v4 offset:8768
	ds_read_b128 v[96:99], v4 offset:8832
	ds_read_b128 v[100:103], v4 offset:8896
	ds_read_b128 v[144:147], v5
	ds_read_b32 v138, v6 offset:128
	ds_read_b32 v139, v6 offset:192
	ds_read_b128 v[104:107], v4 offset:13056
	ds_read_b128 v[108:111], v4 offset:13120
	ds_read_b128 v[112:115], v4 offset:13184
	ds_read_b128 v[116:119], v4 offset:13248
	v_add_u32_e32 v10, 32, v0
	v_lshl_add_u32 v12, v1, 2, s9
	v_add_u32_e32 v13, 1, v12
	v_add_u32_e32 v14, 2, v12
	v_add_u32_e32 v15, 3, v12
	v_mov_b32_e32 v148, 0
	v_mov_b32_e32 v149, 0
	v_mov_b32_e32 v150, 0
	v_mov_b32_e32 v151, 0
	v_mov_b32_e32 v152, 0
	v_mov_b32_e32 v153, 0
	v_mov_b32_e32 v154, 0
	v_mov_b32_e32 v155, 0
	s_waitcnt lgkmcnt(5)
	v_mfma_f32_16x16x32_bf16 v[128:131], v[40:43], v[88:91], 0
	v_mfma_f32_16x16x32_bf16 v[128:131], v[44:47], v[92:95], v[128:131]
	v_mfma_f32_16x16x32_bf16 v[128:131], v[48:51], v[96:99], v[128:131]
	v_mfma_f32_16x16x32_bf16 v[128:131], v[52:55], v[100:103], v[128:131]
	v_sub_f32_e32 v156, v144, v138
	v_sub_f32_e32 v157, v145, v138
	v_sub_f32_e32 v158, v146, v138
	v_sub_f32_e32 v159, v147, v138
	v_mul_f32_e32 v156, s34, v156
	v_mul_f32_e32 v157, s34, v157
	v_mul_f32_e32 v158, s34, v158
	v_mul_f32_e32 v159, s34, v159
	v_exp_f32_e32 v156, v156
	v_exp_f32_e32 v157, v157
	v_exp_f32_e32 v158, v158
	v_exp_f32_e32 v159, v159
	s_waitcnt lgkmcnt(0)
	v_mfma_f32_16x16x32_bf16 v[132:135], v[40:43], v[104:107], 0
	v_mfma_f32_16x16x32_bf16 v[132:135], v[44:47], v[108:111], v[132:135]
	v_mfma_f32_16x16x32_bf16 v[132:135], v[48:51], v[112:115], v[132:135]
	v_mfma_f32_16x16x32_bf16 v[132:135], v[52:55], v[116:119], v[132:135]
	v_mul_f32_e32 v156, v128, v156
	v_mul_f32_e32 v157, v129, v157
	v_mul_f32_e32 v158, v130, v158
	v_mul_f32_e32 v159, v131, v159
	v_cmp_le_i32_e32 vcc, v12, v10
	v_cmp_le_i32_e64 s[0:1], v13, v10
	v_cmp_le_i32_e64 s[20:21], v14, v10
	v_cndmask_b32_e32 v156, 0, v156, vcc
	v_cmp_le_i32_e32 vcc, v15, v10
	v_cndmask_b32_e64 v157, 0, v157, s[0:1]
	v_cndmask_b32_e64 v158, 0, v158, s[20:21]
	s_nop 0
	v_cndmask_b32_e32 v159, 0, v159, vcc
	v_sub_f32_e32 v160, v144, v139
	v_sub_f32_e32 v161, v145, v139
	v_sub_f32_e32 v162, v146, v139
	v_sub_f32_e32 v163, v147, v139
	v_mul_f32_e32 v160, s34, v160
	v_mul_f32_e32 v161, s34, v161
	v_mul_f32_e32 v162, s34, v162
	v_mul_f32_e32 v163, s34, v163
	v_exp_f32_e32 v160, v160
	v_exp_f32_e32 v161, v161
	v_exp_f32_e32 v162, v162
	v_exp_f32_e32 v163, v163
	v_mul_f32_e32 v160, v132, v160
	v_mul_f32_e32 v161, v133, v161
	v_mul_f32_e32 v162, v134, v162
	v_mul_f32_e32 v163, v135, v163
	s_branch .Lgc_st1
.Lgc_v1_3:
	ds_read_b128 v[104:107], v4 offset:13056
	ds_read_b128 v[108:111], v4 offset:13120
	ds_read_b128 v[112:115], v4 offset:13184
	ds_read_b128 v[116:119], v4 offset:13248
	ds_read_b128 v[144:147], v5
	ds_read_b32 v139, v6 offset:192
	v_add_u32_e32 v11, 48, v0
	v_lshl_add_u32 v12, v1, 2, s9
	v_add_u32_e32 v13, 1, v12
	v_add_u32_e32 v14, 2, v12
	v_add_u32_e32 v15, 3, v12
	v_mov_b32_e32 v148, 0
	v_mov_b32_e32 v149, 0
	v_mov_b32_e32 v150, 0
	v_mov_b32_e32 v151, 0
	v_mov_b32_e32 v152, 0
	v_mov_b32_e32 v153, 0
	v_mov_b32_e32 v154, 0
	v_mov_b32_e32 v155, 0
	v_mov_b32_e32 v156, 0
	v_mov_b32_e32 v157, 0
	v_mov_b32_e32 v158, 0
	v_mov_b32_e32 v159, 0
	s_waitcnt lgkmcnt(0)
	v_mfma_f32_16x16x32_bf16 v[132:135], v[40:43], v[104:107], 0
	v_mfma_f32_16x16x32_bf16 v[132:135], v[44:47], v[108:111], v[132:135]
	v_mfma_f32_16x16x32_bf16 v[132:135], v[48:51], v[112:115], v[132:135]
	v_mfma_f32_16x16x32_bf16 v[132:135], v[52:55], v[116:119], v[132:135]
	v_sub_f32_e32 v160, v144, v139
	v_sub_f32_e32 v161, v145, v139
	v_sub_f32_e32 v162, v146, v139
	v_sub_f32_e32 v163, v147, v139
	v_mul_f32_e32 v160, s34, v160
	v_mul_f32_e32 v161, s34, v161
	v_mul_f32_e32 v162, s34, v162
	v_mul_f32_e32 v163, s34, v163
	v_exp_f32_e32 v160, v160
	v_exp_f32_e32 v161, v161
	v_exp_f32_e32 v162, v162
	v_exp_f32_e32 v163, v163
	v_mul_f32_e32 v160, v132, v160
	v_mul_f32_e32 v161, v133, v161
	v_mul_f32_e32 v162, v134, v162
	v_mul_f32_e32 v163, v135, v163
	v_cmp_le_i32_e32 vcc, v12, v11
	v_cmp_le_i32_e64 s[0:1], v13, v11
	v_cmp_le_i32_e64 s[20:21], v14, v11
	v_cndmask_b32_e32 v160, 0, v160, vcc
	v_cmp_le_i32_e32 vcc, v15, v11
	v_cndmask_b32_e64 v161, 0, v161, s[0:1]
	v_cndmask_b32_e64 v162, 0, v162, s[20:21]
	s_nop 0
	v_cndmask_b32_e32 v163, 0, v163, vcc
	s_branch .Lgc_st1
.Lgc_st0:
	v_mul_u32_u24_e32 v16, 0x110, v0
	s_lshl_b32 s34, s9, 2
	s_add_i32 s34, s34, 0x15c00
	v_lshl_add_u32 v16, v1, 4, v16
	v_add_u32_e32 v16, s34, v16
	ds_write_b128 v16, v[148:151]
	ds_write_b128 v16, v[152:155] offset:4352
	ds_write_b128 v16, v[156:159] offset:8704
	ds_write_b128 v16, v[160:163] offset:13056
	s_cmp_lt_u32 s9, 32
	s_cbranch_scc1 .Lgc_join
	s_mul_i32 s34, s9, 0x50
	s_add_i32 s34, s34, 0x1be00
	v_mul_u32_u24_e32 v17, 0x140, v1
	v_lshl_add_u32 v17, v0, 1, v17
	v_add_u32_e32 v17, s34, v17
	v_cvt_pk_bf16_f32 v164, v148, v148
	v_cvt_pk_bf16_f32 v165, v149, v149
	v_cvt_pk_bf16_f32 v166, v150, v150
	v_cvt_pk_bf16_f32 v167, v151, v151
	v_cvt_pk_bf16_f32 v168, v152, v152
	v_cvt_pk_bf16_f32 v169, v153, v153
	v_cvt_pk_bf16_f32 v170, v154, v154
	v_cvt_pk_bf16_f32 v171, v155, v155
	ds_write_b16 v17, v164
	ds_write_b16 v17, v165 offset:80
	ds_write_b16 v17, v166 offset:160
	ds_write_b16 v17, v167 offset:240
	ds_write_b16 v17, v168 offset:32
	ds_write_b16 v17, v169 offset:112
	ds_write_b16 v17, v170 offset:192
	ds_write_b16 v17, v171 offset:272
	s_branch .Lgc_join
.Lgc_st1:
	s_add_u32 s2, s78, 0xc000
	s_addc_u32 s3, s79, 0
	s_lshl_b32 s34, s9, 6
	v_lshlrev_b32_e32 v16, 4, v0
	v_and_b32_e32 v17, 1, v1
	v_lshl_add_u32 v16, v17, 9, v16
	v_lshrrev_b32_e32 v17, 1, v1
	v_lshl_add_u32 v16, v17, 3, v16
	v_add_u32_e32 v16, s34, v16
	v_add_u32_e32 v17, 0x1000, v16
	v_cvt_pk_bf16_f32 v164, v148, v149
	v_cvt_pk_bf16_f32 v165, v150, v151
	v_cvt_pk_bf16_f32 v166, v152, v153
	v_cvt_pk_bf16_f32 v167, v154, v155
	v_cvt_pk_bf16_f32 v168, v156, v157
	v_cvt_pk_bf16_f32 v169, v158, v159
	v_cvt_pk_bf16_f32 v170, v160, v161
	v_cvt_pk_bf16_f32 v171, v162, v163
	global_store_dwordx2 v16, v[164:165], s[2:3]
	global_store_dwordx2 v16, v[166:167], s[2:3] offset:256
	global_store_dwordx2 v17, v[168:169], s[2:3]
	global_store_dwordx2 v17, v[170:171], s[2:3] offset:256
